# MoE tile table: the 16 expert-counter loads of thread 0 issued together (one wait) instead of 16 dependent round trips
# speedup vs baseline: 1.0049x; 1.0002x over previous
.LBB0_1820:
	s_cmp_lt_i32 s42, 10
	s_cselect_b64 s[4:5], -1, 0
	s_cmp_gt_i32 s43, 9
	s_cselect_b64 s[6:7], -1, 0
	s_and_b64 s[4:5], s[4:5], s[6:7]
	s_andn2_b64 vcc, exec, s[4:5]
	s_cbranch_vccnz .LBB0_2037
	v_mov_b32 v1, v0
	s_waitcnt vmcnt(16) lgkmcnt(0)
	v_cmp_eq_u32_e32 vcc, 0, v1
	s_barrier
	s_and_saveexec_b64 s[4:5], vcc
	s_cbranch_execz .LBB0_1823
	v_mov_b32_e32 v1, 0
	v_mov_b32_e32 v4, 0x1000
	global_load_dword v10, v1, s[40:41] offset:256 sc1
	global_load_dword v11, v1, s[40:41] offset:512 sc1
	global_load_dword v12, v1, s[40:41] offset:768 sc1
	global_load_dword v13, v1, s[40:41] offset:1024 sc1
	global_load_dword v14, v1, s[40:41] offset:1280 sc1
	global_load_dword v15, v1, s[40:41] offset:1536 sc1
	global_load_dword v16, v1, s[40:41] offset:1792 sc1
	global_load_dword v17, v1, s[40:41] offset:2048 sc1
	global_load_dword v18, v1, s[40:41] offset:2304 sc1
	global_load_dword v19, v1, s[40:41] offset:2560 sc1
	global_load_dword v20, v1, s[40:41] offset:2816 sc1
	global_load_dword v21, v1, s[40:41] offset:3072 sc1
	global_load_dword v22, v1, s[40:41] offset:3328 sc1
	global_load_dword v23, v1, s[40:41] offset:3584 sc1
	global_load_dword v24, v1, s[40:41] offset:3840 sc1
	global_load_dword v25, v4, s[40:41] sc1
	s_add_i32 s6, 0, 0x20000
	v_mov_b32_e32 v5, s6
	v_mov_b32_e32 v26, 0
	s_waitcnt vmcnt(0)
	ds_write_b32 v5, v10
	ds_write_b32 v5, v26 offset:64
	v_add_u32_e32 v27, 0xff, v10
	v_ashrrev_i32_e32 v27, 8, v27
	v_add_u32_e32 v26, v27, v26
	ds_write_b32 v5, v11 offset:4
	ds_write_b32 v5, v26 offset:68
	v_add_u32_e32 v27, 0xff, v11
	v_ashrrev_i32_e32 v27, 8, v27
	v_add_u32_e32 v26, v27, v26
	ds_write_b32 v5, v12 offset:8
	ds_write_b32 v5, v26 offset:72
	v_add_u32_e32 v27, 0xff, v12
	v_ashrrev_i32_e32 v27, 8, v27
	v_add_u32_e32 v26, v27, v26
	ds_write_b32 v5, v13 offset:12
	ds_write_b32 v5, v26 offset:76
	v_add_u32_e32 v27, 0xff, v13
	v_ashrrev_i32_e32 v27, 8, v27
	v_add_u32_e32 v26, v27, v26
	ds_write_b32 v5, v14 offset:16
	ds_write_b32 v5, v26 offset:80
	v_add_u32_e32 v27, 0xff, v14
	v_ashrrev_i32_e32 v27, 8, v27
	v_add_u32_e32 v26, v27, v26
	ds_write_b32 v5, v15 offset:20
	ds_write_b32 v5, v26 offset:84
	v_add_u32_e32 v27, 0xff, v15
	v_ashrrev_i32_e32 v27, 8, v27
	v_add_u32_e32 v26, v27, v26
	ds_write_b32 v5, v16 offset:24
	ds_write_b32 v5, v26 offset:88
	v_add_u32_e32 v27, 0xff, v16
	v_ashrrev_i32_e32 v27, 8, v27
	v_add_u32_e32 v26, v27, v26
	ds_write_b32 v5, v17 offset:28
	ds_write_b32 v5, v26 offset:92
	v_add_u32_e32 v27, 0xff, v17
	v_ashrrev_i32_e32 v27, 8, v27
	v_add_u32_e32 v26, v27, v26
	ds_write_b32 v5, v18 offset:32
	ds_write_b32 v5, v26 offset:96
	v_add_u32_e32 v27, 0xff, v18
	v_ashrrev_i32_e32 v27, 8, v27
	v_add_u32_e32 v26, v27, v26
	ds_write_b32 v5, v19 offset:36
	ds_write_b32 v5, v26 offset:100
	v_add_u32_e32 v27, 0xff, v19
	v_ashrrev_i32_e32 v27, 8, v27
	v_add_u32_e32 v26, v27, v26
	ds_write_b32 v5, v20 offset:40
	ds_write_b32 v5, v26 offset:104
	v_add_u32_e32 v27, 0xff, v20
	v_ashrrev_i32_e32 v27, 8, v27
	v_add_u32_e32 v26, v27, v26
	ds_write_b32 v5, v21 offset:44
	ds_write_b32 v5, v26 offset:108
	v_add_u32_e32 v27, 0xff, v21
	v_ashrrev_i32_e32 v27, 8, v27
	v_add_u32_e32 v26, v27, v26
	ds_write_b32 v5, v22 offset:48
	ds_write_b32 v5, v26 offset:112
	v_add_u32_e32 v27, 0xff, v22
	v_ashrrev_i32_e32 v27, 8, v27
	v_add_u32_e32 v26, v27, v26
	ds_write_b32 v5, v23 offset:52
	ds_write_b32 v5, v26 offset:116
	v_add_u32_e32 v27, 0xff, v23
	v_ashrrev_i32_e32 v27, 8, v27
	v_add_u32_e32 v26, v27, v26
	ds_write_b32 v5, v24 offset:56
	ds_write_b32 v5, v26 offset:120
	v_add_u32_e32 v27, 0xff, v24
	v_ashrrev_i32_e32 v27, 8, v27
	v_add_u32_e32 v26, v27, v26
	ds_write_b32 v5, v25 offset:60
	ds_write_b32 v5, v26 offset:124
	v_add_u32_e32 v27, 0xff, v25
	v_ashrrev_i32_e32 v27, 8, v27
	v_add_u32_e32 v26, v27, v26
	ds_write_b32 v5, v26 offset:128

.LBB0_3324:
	s_cmp_lt_i32 s42, 20
	s_cselect_b64 s[4:5], -1, 0
	s_cmp_gt_i32 s43, 19
	s_cselect_b64 s[6:7], -1, 0
	s_and_b64 s[4:5], s[4:5], s[6:7]
	s_andn2_b64 vcc, exec, s[4:5]
	s_cbranch_vccnz .LBB0_3541
	v_mov_b32 v1, v0
	s_waitcnt vmcnt(0) lgkmcnt(0)
	v_cmp_eq_u32_e32 vcc, 0, v1
	s_barrier
	s_and_saveexec_b64 s[4:5], vcc
	s_cbranch_execz .LBB0_3327
	v_mov_b32_e32 v1, 0x1000
	v_mov_b32_e32 v4, 0x2000
	global_load_dword v10, v1, s[40:41] offset:256 sc1
	global_load_dword v11, v1, s[40:41] offset:512 sc1
	global_load_dword v12, v1, s[40:41] offset:768 sc1
	global_load_dword v13, v1, s[40:41] offset:1024 sc1
	global_load_dword v14, v1, s[40:41] offset:1280 sc1
	global_load_dword v15, v1, s[40:41] offset:1536 sc1
	global_load_dword v16, v1, s[40:41] offset:1792 sc1
	global_load_dword v17, v1, s[40:41] offset:2048 sc1
	global_load_dword v18, v1, s[40:41] offset:2304 sc1
	global_load_dword v19, v1, s[40:41] offset:2560 sc1
	global_load_dword v20, v1, s[40:41] offset:2816 sc1
	global_load_dword v21, v1, s[40:41] offset:3072 sc1
	global_load_dword v22, v1, s[40:41] offset:3328 sc1
	global_load_dword v23, v1, s[40:41] offset:3584 sc1
	global_load_dword v24, v1, s[40:41] offset:3840 sc1
	global_load_dword v25, v4, s[40:41] sc1
	s_add_i32 s6, 0, 0x20000
	v_mov_b32_e32 v5, s6
	v_mov_b32_e32 v26, 0
	s_waitcnt vmcnt(0)
	ds_write_b32 v5, v10
	ds_write_b32 v5, v26 offset:64
	v_add_u32_e32 v27, 0xff, v10
	v_ashrrev_i32_e32 v27, 8, v27
	v_add_u32_e32 v26, v27, v26
	ds_write_b32 v5, v11 offset:4
	ds_write_b32 v5, v26 offset:68
	v_add_u32_e32 v27, 0xff, v11
	v_ashrrev_i32_e32 v27, 8, v27
	v_add_u32_e32 v26, v27, v26
	ds_write_b32 v5, v12 offset:8
	ds_write_b32 v5, v26 offset:72
	v_add_u32_e32 v27, 0xff, v12
	v_ashrrev_i32_e32 v27, 8, v27
	v_add_u32_e32 v26, v27, v26
	ds_write_b32 v5, v13 offset:12
	ds_write_b32 v5, v26 offset:76
	v_add_u32_e32 v27, 0xff, v13
	v_ashrrev_i32_e32 v27, 8, v27
	v_add_u32_e32 v26, v27, v26
	ds_write_b32 v5, v14 offset:16
	ds_write_b32 v5, v26 offset:80
	v_add_u32_e32 v27, 0xff, v14
	v_ashrrev_i32_e32 v27, 8, v27
	v_add_u32_e32 v26, v27, v26
	ds_write_b32 v5, v15 offset:20
	ds_write_b32 v5, v26 offset:84
	v_add_u32_e32 v27, 0xff, v15
	v_ashrrev_i32_e32 v27, 8, v27
	v_add_u32_e32 v26, v27, v26
	ds_write_b32 v5, v16 offset:24
	ds_write_b32 v5, v26 offset:88
	v_add_u32_e32 v27, 0xff, v16
	v_ashrrev_i32_e32 v27, 8, v27
	v_add_u32_e32 v26, v27, v26
	ds_write_b32 v5, v17 offset:28
	ds_write_b32 v5, v26 offset:92
	v_add_u32_e32 v27, 0xff, v17
	v_ashrrev_i32_e32 v27, 8, v27
	v_add_u32_e32 v26, v27, v26
	ds_write_b32 v5, v18 offset:32
	ds_write_b32 v5, v26 offset:96
	v_add_u32_e32 v27, 0xff, v18
	v_ashrrev_i32_e32 v27, 8, v27
	v_add_u32_e32 v26, v27, v26
	ds_write_b32 v5, v19 offset:36
	ds_write_b32 v5, v26 offset:100
	v_add_u32_e32 v27, 0xff, v19
	v_ashrrev_i32_e32 v27, 8, v27
	v_add_u32_e32 v26, v27, v26
	ds_write_b32 v5, v20 offset:40
	ds_write_b32 v5, v26 offset:104
	v_add_u32_e32 v27, 0xff, v20
	v_ashrrev_i32_e32 v27, 8, v27
	v_add_u32_e32 v26, v27, v26
	ds_write_b32 v5, v21 offset:44
	ds_write_b32 v5, v26 offset:108
	v_add_u32_e32 v27, 0xff, v21
	v_ashrrev_i32_e32 v27, 8, v27
	v_add_u32_e32 v26, v27, v26
	ds_write_b32 v5, v22 offset:48
	ds_write_b32 v5, v26 offset:112
	v_add_u32_e32 v27, 0xff, v22
	v_ashrrev_i32_e32 v27, 8, v27
	v_add_u32_e32 v26, v27, v26
	ds_write_b32 v5, v23 offset:52
	ds_write_b32 v5, v26 offset:116
	v_add_u32_e32 v27, 0xff, v23
	v_ashrrev_i32_e32 v27, 8, v27
	v_add_u32_e32 v26, v27, v26
	ds_write_b32 v5, v24 offset:56
	ds_write_b32 v5, v26 offset:120
	v_add_u32_e32 v27, 0xff, v24
	v_ashrrev_i32_e32 v27, 8, v27
	v_add_u32_e32 v26, v27, v26
	ds_write_b32 v5, v25 offset:60
	ds_write_b32 v5, v26 offset:124
	v_add_u32_e32 v27, 0xff, v25
	v_ashrrev_i32_e32 v27, 8, v27
	v_add_u32_e32 v26, v27, v26
	ds_write_b32 v5, v26 offset:128
